# adds nontemporal hint to the indexer score tile stores (f16 score matrix, written once, streamed) on top of FINAL-phase nt
# speedup vs baseline: 1.0064x; 1.0051x over previous
.LBB0_405:
	s_add_i32 s18, s18, -1
	s_bitcmp1_b32 s18, 0
	s_cselect_b32 s0, 0x4200, 0
	v_add_u32_e32 v6, s0, v151
	ds_read_b128 v[2:5], v6 offset:36864
	ds_read_b128 v[6:9], v6 offset:36880
	s_lshl_b32 s0, s18, 7
	v_lshl_add_u64 v[10:11], s[88:89], 0, v[140:141]
	s_ashr_i32 s1, s0, 31
	v_lshl_add_u64 v[10:11], s[0:1], 1, v[10:11]
	v_lshlrev_b32_e32 v12, 1, v96
	v_mov_b32_e32 v13, v91
	v_lshl_add_u64 v[14:15], v[10:11], 0, v[12:13]
	s_waitcnt lgkmcnt(1)
	v_cvt_pkrtz_f16_f32 v10, v2, v3
	v_max_f32_e32 v3, v3, v3
	v_max_f32_e32 v2, v2, v2
	v_cvt_pkrtz_f16_f32 v11, v4, v5
	v_max_f32_e32 v2, v2, v3
	v_max_f32_e32 v3, v5, v5
	v_max_f32_e32 v4, v4, v4
	v_max_f32_e32 v3, v4, v3
	s_waitcnt lgkmcnt(0)
	v_max_f32_e32 v4, v9, v9
	v_max_f32_e32 v5, v8, v8
	v_max_f32_e32 v4, v5, v4
	v_max3_f32 v4, v6, v7, v4
	v_max3_f32 v2, v2, v3, v4
	s_lshl_b32 s0, s18, 4
	v_cvt_pkrtz_f16_f32 v12, v6, v7
	v_cvt_pkrtz_f16_f32 v6, v2, v2
	s_ashr_i32 s1, s0, 31
	v_lshl_add_u64 v[2:3], s[52:53], 0, v[138:139]
	v_lshl_add_u64 v[2:3], s[0:1], 1, v[2:3]
	v_lshlrev_b32_e32 v4, 1, v94
	v_mov_b32_e32 v5, v91
	v_cvt_pkrtz_f16_f32 v13, v8, v9
	v_lshl_add_u64 v[2:3], v[2:3], 0, v[4:5]
	global_store_dwordx4 v[14:15], v[10:13], off nt
	global_store_short v[2:3], v6, off
	s_barrier

.LBB0_425:
	s_add_i32 s55, s1, 1
	s_cmp_le_i32 s55, s34
	s_cbranch_scc1 .LBB0_427
	s_bitcmp1_b32 s1, 0
	s_cselect_b32 s1, 0x4200, 0
	v_add_u32_e32 v6, s1, v151
	ds_read_b128 v[2:5], v6 offset:36864
	ds_read_b128 v[6:9], v6 offset:36880
	s_ashr_i32 s17, s16, 31
	s_ashr_i32 s1, s0, 31
	v_lshl_add_u64 v[14:15], s[16:17], 1, v[142:143]
	s_waitcnt lgkmcnt(1)
	v_cvt_pkrtz_f16_f32 v10, v2, v3
	v_max_f32_e32 v3, v3, v3
	v_max_f32_e32 v2, v2, v2
	v_cvt_pkrtz_f16_f32 v11, v4, v5
	v_max_f32_e32 v2, v2, v3
	v_max_f32_e32 v3, v5, v5
	v_max_f32_e32 v4, v4, v4
	v_max_f32_e32 v3, v4, v3
	s_waitcnt lgkmcnt(0)
	v_max_f32_e32 v4, v9, v9
	v_max_f32_e32 v5, v8, v8
	v_max_f32_e32 v4, v5, v4
	v_max3_f32 v4, v6, v7, v4
	v_max3_f32 v2, v2, v3, v4
	v_cvt_pkrtz_f16_f32 v12, v6, v7
	v_cvt_pkrtz_f16_f32 v13, v8, v9
	v_cvt_pkrtz_f16_f32 v4, v2, v2
	v_lshl_add_u64 v[2:3], s[0:1], 1, v[144:145]
	global_store_dwordx4 v[14:15], v[10:13], off nt
	global_store_short v[2:3], v4, off

.LBB0_432:
	s_add_i32 s43, s43, -1
	s_bitcmp1_b32 s43, 0
	s_cselect_b32 s0, 0x4200, 0
	v_add_u32_e32 v6, s0, v151
	ds_read_b128 v[2:5], v6 offset:36864
	ds_read_b128 v[6:9], v6 offset:36880
	s_lshl_b32 s0, s43, 7
	v_lshl_add_u64 v[10:11], s[88:89], 0, v[140:141]
	s_ashr_i32 s1, s0, 31
	v_lshl_add_u64 v[10:11], s[0:1], 1, v[10:11]
	v_lshlrev_b32_e32 v12, 1, v96
	v_mov_b32_e32 v13, v91
	v_lshl_add_u64 v[14:15], v[10:11], 0, v[12:13]
	s_waitcnt lgkmcnt(1)
	v_cvt_pkrtz_f16_f32 v10, v2, v3
	v_max_f32_e32 v3, v3, v3
	v_max_f32_e32 v2, v2, v2
	v_cvt_pkrtz_f16_f32 v11, v4, v5
	v_max_f32_e32 v2, v2, v3
	v_max_f32_e32 v3, v5, v5
	v_max_f32_e32 v4, v4, v4
	v_max_f32_e32 v3, v4, v3
	s_waitcnt lgkmcnt(0)
	v_max_f32_e32 v4, v9, v9
	v_max_f32_e32 v5, v8, v8
	v_max_f32_e32 v4, v5, v4
	v_max3_f32 v4, v6, v7, v4
	v_max3_f32 v2, v2, v3, v4
	s_lshl_b32 s0, s43, 4
	v_cvt_pkrtz_f16_f32 v12, v6, v7
	v_cvt_pkrtz_f16_f32 v6, v2, v2
	s_ashr_i32 s1, s0, 31
	v_lshl_add_u64 v[2:3], s[52:53], 0, v[138:139]
	v_lshl_add_u64 v[2:3], s[0:1], 1, v[2:3]
	v_lshlrev_b32_e32 v4, 1, v94
	v_mov_b32_e32 v5, v91
	v_cvt_pkrtz_f16_f32 v13, v8, v9
	v_lshl_add_u64 v[2:3], v[2:3], 0, v[4:5]
	global_store_dwordx4 v[14:15], v[10:13], off nt
	global_store_short v[2:3], v6, off
	s_barrier
	s_max_i32 s34, s34, s42
	s_cmp_le_i32 s35, s34
	s_cbranch_scc1 .LBB0_406

.LBB0_442:
	s_add_i32 s34, s1, 1
	s_cmp_le_i32 s34, s19
	s_cbranch_scc1 .LBB0_444
	s_bitcmp1_b32 s1, 0
	s_cselect_b32 s1, 0x4200, 0
	v_add_u32_e32 v6, s1, v151
	ds_read_b128 v[2:5], v6 offset:36864
	ds_read_b128 v[6:9], v6 offset:36880
	s_add_i32 s42, s29, 0xffffff00
	s_ashr_i32 s43, s42, 31
	s_ashr_i32 s1, s0, 31
	s_waitcnt lgkmcnt(1)
	v_cvt_pkrtz_f16_f32 v10, v2, v3
	v_max_f32_e32 v3, v3, v3
	v_max_f32_e32 v2, v2, v2
	v_cvt_pkrtz_f16_f32 v11, v4, v5
	v_max_f32_e32 v2, v2, v3
	v_max_f32_e32 v3, v5, v5
	v_max_f32_e32 v4, v4, v4
	v_max_f32_e32 v3, v4, v3
	s_waitcnt lgkmcnt(0)
	v_max_f32_e32 v4, v9, v9
	v_max_f32_e32 v5, v8, v8
	v_max_f32_e32 v4, v5, v4
	v_max3_f32 v4, v6, v7, v4
	v_max3_f32 v2, v2, v3, v4
	v_lshl_add_u64 v[14:15], s[42:43], 1, v[142:143]
	v_cvt_pkrtz_f16_f32 v12, v6, v7
	v_cvt_pkrtz_f16_f32 v13, v8, v9
	v_cvt_pkrtz_f16_f32 v4, v2, v2
	v_lshl_add_u64 v[2:3], s[0:1], 1, v[144:145]
	global_store_dwordx4 v[14:15], v[10:13], off nt
	global_store_short v[2:3], v4, off
